# v13 + nt policy on the P2 projection GEMM epilogue stores (318 MB PROJ output stream no longer evicts operand tiles from L2)
# speedup vs baseline: 1.0473x; 1.0111x over previous
.LBB0_215:
	v_mov_b32_e32 v130, v183
	v_cvt_pk_bf16_f32 v126, v126, v127
	v_cvt_pk_bf16_f32 v127, v128, v129
	v_cvt_pk_bf16_f32 v128, v122, v123
	v_cvt_pk_bf16_f32 v129, v124, v125
	v_cvt_pk_bf16_f32 v118, v118, v119
	s_nop 0
	v_and_b32_e32 v132, 7, v130
	v_lshlrev_b32_e32 v133, 7, v130
	v_lshrrev_b32_e32 v134, 3, v130
	v_and_b32_e32 v133, 0x780, v133
	v_bitop3_b32 v134, v134, v132, s57 bitop3:0x6c
	v_ashrrev_i32_e32 v131, 3, v130
	v_add_u32_e32 v133, s39, v133
	v_lshlrev_b32_e32 v134, 4, v134
	v_lshlrev_b32_e32 v135, 7, v131
	v_bitop3_b32 v130, v130, v131, 7 bitop3:0x6c
	v_add_u32_e32 v131, v133, v134
	v_lshlrev_b32_e32 v130, 4, v130
	ds_write_b128 v131, v[126:129]
	v_xad_u32 v126, v134, 16, v133
	v_add3_u32 v130, s39, v135, v130
	v_cvt_pk_bf16_f32 v119, v120, v121
	v_cvt_pk_bf16_f32 v120, v110, v111
	v_cvt_pk_bf16_f32 v121, v112, v113
	ds_write_b128 v126, v[118:121]
	ds_read_b128 v[118:121], v130
	ds_read_b128 v[122:125], v130 offset:1024
	v_lshl_or_b32 v112, v132, 4, s54
	v_mov_b32_e32 v113, v173
	v_lshl_add_u64 v[110:111], s[4:5], 0, v[112:113]
	s_waitcnt lgkmcnt(0)
	global_store_dwordx4 v112, v[118:121], s[4:5] nt
	v_add_co_u32_e32 v112, vcc, s58, v110
	v_cvt_pk_bf16_f32 v102, v102, v103
	v_cvt_pk_bf16_f32 v103, v104, v105
	v_cvt_pk_bf16_f32 v104, v94, v95
	v_cvt_pk_bf16_f32 v105, v96, v97
	s_nop 1
	v_addc_co_u32_e32 v113, vcc, 0, v111, vcc
	global_store_dwordx4 v[112:113], v[122:125], off nt
	v_cvt_pk_bf16_f32 v112, v114, v115
	v_cvt_pk_bf16_f32 v113, v116, v117
	v_cvt_pk_bf16_f32 v114, v106, v107
	v_cvt_pk_bf16_f32 v115, v108, v109
	ds_write_b128 v131, v[112:115]
	ds_write_b128 v126, v[102:105]
	ds_read_b128 v[94:97], v130
	ds_read_b128 v[102:105], v130 offset:1024
	v_add_co_u32_e32 v106, vcc, s59, v110
	v_cvt_pk_bf16_f32 v86, v86, v87
	v_cvt_pk_bf16_f32 v87, v88, v89
	v_cvt_pk_bf16_f32 v88, v78, v79
	v_cvt_pk_bf16_f32 v89, v80, v81
	s_nop 1
	v_addc_co_u32_e32 v107, vcc, 0, v111, vcc
	s_waitcnt lgkmcnt(0)
	global_store_dwordx4 v[106:107], v[94:97], off nt
	v_cvt_pk_bf16_f32 v70, v70, v71
	v_cvt_pk_bf16_f32 v71, v72, v73
	v_cvt_pk_bf16_f32 v72, v66, v67
	v_cvt_pk_bf16_f32 v73, v68, v69
	v_cvt_pk_bf16_f32 v62, v62, v63
	s_nop 1
	v_add_co_u32_e32 v94, vcc, s60, v110
	v_cvt_pk_bf16_f32 v96, v90, v91
	v_cvt_pk_bf16_f32 v97, v92, v93
	v_cvt_pk_bf16_f32 v63, v64, v65
	v_cvt_pk_bf16_f32 v64, v58, v59
	s_nop 1
	v_addc_co_u32_e32 v95, vcc, 0, v111, vcc
	global_store_dwordx4 v[94:95], v[102:105], off nt
	v_cvt_pk_bf16_f32 v94, v98, v99
	v_cvt_pk_bf16_f32 v95, v100, v101
	ds_write_b128 v131, v[94:97]
	ds_write_b128 v126, v[86:89]
	ds_read_b128 v[78:81], v130
	ds_read_b128 v[86:89], v130 offset:1024
	v_add_co_u32_e32 v90, vcc, s61, v110
	v_cvt_pk_bf16_f32 v65, v60, v61
	v_cvt_pk_bf16_f32 v54, v54, v55
	v_cvt_pk_bf16_f32 v55, v56, v57
	v_cvt_pk_bf16_f32 v56, v46, v47
	s_nop 1
	v_addc_co_u32_e32 v91, vcc, 0, v111, vcc
	s_waitcnt lgkmcnt(0)
	global_store_dwordx4 v[90:91], v[78:81], off nt
	v_cvt_pk_bf16_f32 v57, v48, v49
	v_cvt_pk_bf16_f32 v38, v38, v39
	v_cvt_pk_bf16_f32 v39, v40, v41
	v_cvt_pk_bf16_f32 v40, v30, v31
	v_cvt_pk_bf16_f32 v41, v32, v33
	s_nop 1
	v_add_co_u32_e32 v78, vcc, s62, v110
	v_cvt_pk_bf16_f32 v80, v74, v75
	v_cvt_pk_bf16_f32 v81, v76, v77
	v_cvt_pk_bf16_f32 v22, v22, v23
	v_cvt_pk_bf16_f32 v23, v24, v25
	s_nop 1
	v_addc_co_u32_e32 v79, vcc, 0, v111, vcc
	global_store_dwordx4 v[78:79], v[86:89], off nt
	v_cvt_pk_bf16_f32 v78, v82, v83
	v_cvt_pk_bf16_f32 v79, v84, v85
	ds_write_b128 v131, v[78:81]
	ds_write_b128 v126, v[70:73]
	ds_read_b128 v[66:69], v130
	ds_read_b128 v[70:73], v130 offset:1024
	v_add_co_u32_e32 v74, vcc, s63, v110
	ds_write_b128 v131, v[62:65]
	s_nop 0
	v_addc_co_u32_e32 v75, vcc, 0, v111, vcc
	s_waitcnt lgkmcnt(0)
	global_store_dwordx4 v[74:75], v[66:69], off nt
	ds_write_b128 v126, v[54:57]
	v_cvt_pk_bf16_f32 v24, v14, v15
	v_cvt_pk_bf16_f32 v25, v16, v17
	v_cvt_pk_bf16_f32 v6, v6, v7
	v_cvt_pk_bf16_f32 v7, v8, v9
	s_nop 0
	v_add_co_u32_e32 v66, vcc, s64, v110
	v_cvt_pk_bf16_f32 v8, v2, v3
	v_cvt_pk_bf16_f32 v9, v4, v5
	s_mov_b64 s[0:1], -1
	s_nop 0
	v_addc_co_u32_e32 v67, vcc, 0, v111, vcc
	global_store_dwordx4 v[66:67], v[70:73], off nt
	ds_read_b128 v[46:49], v130
	ds_read_b128 v[54:57], v130 offset:1024
	v_add_co_u32_e32 v58, vcc, s65, v110
	s_nop 1
	v_addc_co_u32_e32 v59, vcc, 0, v111, vcc
	s_waitcnt lgkmcnt(0)
	global_store_dwordx4 v[58:59], v[46:49], off nt
	s_nop 1
	v_add_co_u32_e32 v46, vcc, s66, v110
	v_cvt_pk_bf16_f32 v48, v42, v43
	v_cvt_pk_bf16_f32 v49, v44, v45
	s_nop 1
	v_addc_co_u32_e32 v47, vcc, 0, v111, vcc
	global_store_dwordx4 v[46:47], v[54:57], off nt
	v_cvt_pk_bf16_f32 v46, v50, v51
	v_cvt_pk_bf16_f32 v47, v52, v53
	ds_write_b128 v131, v[46:49]
	ds_write_b128 v126, v[38:41]
	ds_read_b128 v[30:33], v130
	ds_read_b128 v[38:41], v130 offset:1024
	v_add_co_u32_e32 v42, vcc, s67, v110
	s_nop 1
	v_addc_co_u32_e32 v43, vcc, 0, v111, vcc
	s_waitcnt lgkmcnt(0)
	global_store_dwordx4 v[42:43], v[30:33], off nt
	s_nop 1
	v_add_co_u32_e32 v30, vcc, s68, v110
	v_cvt_pk_bf16_f32 v32, v26, v27
	v_cvt_pk_bf16_f32 v33, v28, v29
	s_nop 1
	v_addc_co_u32_e32 v31, vcc, 0, v111, vcc
	global_store_dwordx4 v[30:31], v[38:41], off nt
	v_cvt_pk_bf16_f32 v30, v34, v35
	v_cvt_pk_bf16_f32 v31, v36, v37
	ds_write_b128 v131, v[30:33]
	ds_write_b128 v126, v[22:25]
	ds_read_b128 v[14:17], v130
	ds_read_b128 v[22:25], v130 offset:1024
	v_add_co_u32_e32 v26, vcc, s69, v110
	s_nop 1
	v_addc_co_u32_e32 v27, vcc, 0, v111, vcc
	s_waitcnt lgkmcnt(0)
	global_store_dwordx4 v[26:27], v[14:17], off nt
	s_nop 1
	v_add_co_u32_e32 v14, vcc, s70, v110
	v_cvt_pk_bf16_f32 v16, v10, v11
	v_cvt_pk_bf16_f32 v17, v12, v13
	s_nop 1
	v_addc_co_u32_e32 v15, vcc, 0, v111, vcc
	global_store_dwordx4 v[14:15], v[22:25], off nt
	v_cvt_pk_bf16_f32 v14, v18, v19
	v_cvt_pk_bf16_f32 v15, v20, v21
	ds_write_b128 v131, v[14:17]
	ds_write_b128 v126, v[6:9]
	ds_read_b128 v[2:5], v130
	ds_read_b128 v[6:9], v130 offset:1024
	v_add_co_u32_e32 v10, vcc, 0x688000, v110
	s_nop 1
	v_addc_co_u32_e32 v11, vcc, 0, v111, vcc
	s_waitcnt lgkmcnt(0)
	global_store_dwordx4 v[10:11], v[2:5], off nt
	s_nop 1
	v_add_co_u32_e32 v2, vcc, 0x6d4000, v110
	s_nop 1
	v_addc_co_u32_e32 v3, vcc, 0, v111, vcc
	s_andn2_b64 vcc, exec, s[22:23]
	global_store_dwordx4 v[2:3], v[6:9], off nt
	s_cbranch_vccnz .LBB0_203
	s_andn2_b64 vcc, exec, s[8:9]
	s_cbranch_vccnz .LBB0_202
	s_barrier
	s_branch .LBB0_202

.LBB0_348:
	v_mov_b32_e32 v130, v183
	v_cvt_pk_bf16_f32 v126, v126, v127
	v_cvt_pk_bf16_f32 v127, v128, v129
	v_cvt_pk_bf16_f32 v128, v122, v123
	v_cvt_pk_bf16_f32 v129, v124, v125
	v_cvt_pk_bf16_f32 v118, v118, v119
	s_nop 0
	v_and_b32_e32 v132, 7, v130
	v_lshlrev_b32_e32 v133, 7, v130
	v_lshrrev_b32_e32 v134, 3, v130
	v_and_b32_e32 v133, 0x780, v133
	v_bitop3_b32 v134, v134, v132, s65 bitop3:0x6c
	v_ashrrev_i32_e32 v131, 3, v130
	v_add_u32_e32 v133, s39, v133
	v_lshlrev_b32_e32 v134, 4, v134
	v_lshlrev_b32_e32 v135, 7, v131
	v_bitop3_b32 v130, v130, v131, 7 bitop3:0x6c
	v_add_u32_e32 v131, v133, v134
	v_lshlrev_b32_e32 v130, 4, v130
	ds_write_b128 v131, v[126:129]
	v_xad_u32 v126, v134, 16, v133
	v_add3_u32 v130, s39, v135, v130
	v_cvt_pk_bf16_f32 v119, v120, v121
	v_cvt_pk_bf16_f32 v120, v110, v111
	v_cvt_pk_bf16_f32 v121, v112, v113
	ds_write_b128 v126, v[118:121]
	ds_read_b128 v[118:121], v130
	ds_read_b128 v[122:125], v130 offset:1024
	v_lshl_or_b32 v112, v132, 4, s59
	v_mov_b32_e32 v113, v173
	v_lshl_add_u64 v[110:111], s[4:5], 0, v[112:113]
	s_waitcnt lgkmcnt(0)
	global_store_dwordx4 v112, v[118:121], s[4:5] nt
	v_add_co_u32_e32 v112, vcc, s66, v110
	v_cvt_pk_bf16_f32 v102, v102, v103
	v_cvt_pk_bf16_f32 v103, v104, v105
	v_cvt_pk_bf16_f32 v104, v94, v95
	v_cvt_pk_bf16_f32 v105, v96, v97
	s_nop 1
	v_addc_co_u32_e32 v113, vcc, 0, v111, vcc
	global_store_dwordx4 v[112:113], v[122:125], off nt
	v_cvt_pk_bf16_f32 v112, v114, v115
	v_cvt_pk_bf16_f32 v113, v116, v117
	v_cvt_pk_bf16_f32 v114, v106, v107
	v_cvt_pk_bf16_f32 v115, v108, v109
	ds_write_b128 v131, v[112:115]
	ds_write_b128 v126, v[102:105]
	ds_read_b128 v[94:97], v130
	ds_read_b128 v[102:105], v130 offset:1024
	v_add_co_u32_e32 v106, vcc, s67, v110
	v_cvt_pk_bf16_f32 v86, v86, v87
	v_cvt_pk_bf16_f32 v87, v88, v89
	v_cvt_pk_bf16_f32 v88, v78, v79
	v_cvt_pk_bf16_f32 v89, v80, v81
	s_nop 1
	v_addc_co_u32_e32 v107, vcc, 0, v111, vcc
	s_waitcnt lgkmcnt(0)
	global_store_dwordx4 v[106:107], v[94:97], off nt
	v_cvt_pk_bf16_f32 v70, v70, v71
	v_cvt_pk_bf16_f32 v71, v72, v73
	v_cvt_pk_bf16_f32 v72, v66, v67
	v_cvt_pk_bf16_f32 v73, v68, v69
	v_cvt_pk_bf16_f32 v62, v62, v63
	s_nop 1
	v_add_co_u32_e32 v94, vcc, s68, v110
	v_cvt_pk_bf16_f32 v96, v90, v91
	v_cvt_pk_bf16_f32 v97, v92, v93
	v_cvt_pk_bf16_f32 v63, v64, v65
	v_cvt_pk_bf16_f32 v64, v58, v59
	s_nop 1
	v_addc_co_u32_e32 v95, vcc, 0, v111, vcc
	global_store_dwordx4 v[94:95], v[102:105], off nt
	v_cvt_pk_bf16_f32 v94, v98, v99
	v_cvt_pk_bf16_f32 v95, v100, v101
	ds_write_b128 v131, v[94:97]
	ds_write_b128 v126, v[86:89]
	ds_read_b128 v[78:81], v130
	ds_read_b128 v[86:89], v130 offset:1024
	v_add_co_u32_e32 v90, vcc, s69, v110
	v_cvt_pk_bf16_f32 v65, v60, v61
	v_cvt_pk_bf16_f32 v54, v54, v55
	v_cvt_pk_bf16_f32 v55, v56, v57
	v_cvt_pk_bf16_f32 v56, v46, v47
	s_nop 1
	v_addc_co_u32_e32 v91, vcc, 0, v111, vcc
	s_waitcnt lgkmcnt(0)
	global_store_dwordx4 v[90:91], v[78:81], off nt
	v_cvt_pk_bf16_f32 v57, v48, v49
	v_cvt_pk_bf16_f32 v38, v38, v39
	v_cvt_pk_bf16_f32 v39, v40, v41
	v_cvt_pk_bf16_f32 v40, v30, v31
	v_cvt_pk_bf16_f32 v41, v32, v33
	s_nop 1
	v_add_co_u32_e32 v78, vcc, s70, v110
	v_cvt_pk_bf16_f32 v80, v74, v75
	v_cvt_pk_bf16_f32 v81, v76, v77
	v_cvt_pk_bf16_f32 v22, v22, v23
	v_cvt_pk_bf16_f32 v23, v24, v25
	s_nop 1
	v_addc_co_u32_e32 v79, vcc, 0, v111, vcc
	global_store_dwordx4 v[78:79], v[86:89], off nt
	v_cvt_pk_bf16_f32 v78, v82, v83
	v_cvt_pk_bf16_f32 v79, v84, v85
	ds_write_b128 v131, v[78:81]
	ds_write_b128 v126, v[70:73]
	ds_read_b128 v[66:69], v130
	ds_read_b128 v[70:73], v130 offset:1024
	v_add_co_u32_e32 v74, vcc, s71, v110
	ds_write_b128 v131, v[62:65]
	s_nop 0
	v_addc_co_u32_e32 v75, vcc, 0, v111, vcc
	s_waitcnt lgkmcnt(0)
	global_store_dwordx4 v[74:75], v[66:69], off nt
	ds_write_b128 v126, v[54:57]
	v_cvt_pk_bf16_f32 v24, v14, v15
	v_cvt_pk_bf16_f32 v25, v16, v17
	v_cvt_pk_bf16_f32 v6, v6, v7
	v_cvt_pk_bf16_f32 v7, v8, v9
	s_nop 0
	v_add_co_u32_e32 v66, vcc, s72, v110
	v_cvt_pk_bf16_f32 v8, v2, v3
	v_cvt_pk_bf16_f32 v9, v4, v5
	s_mov_b64 s[0:1], -1
	s_nop 0
	v_addc_co_u32_e32 v67, vcc, 0, v111, vcc
	global_store_dwordx4 v[66:67], v[70:73], off nt
	ds_read_b128 v[46:49], v130
	ds_read_b128 v[54:57], v130 offset:1024
	v_add_co_u32_e32 v58, vcc, s73, v110
	s_nop 1
	v_addc_co_u32_e32 v59, vcc, 0, v111, vcc
	s_waitcnt lgkmcnt(0)
	global_store_dwordx4 v[58:59], v[46:49], off nt
	s_nop 1
	v_add_co_u32_e32 v46, vcc, s74, v110
	v_cvt_pk_bf16_f32 v48, v42, v43
	v_cvt_pk_bf16_f32 v49, v44, v45
	s_nop 1
	v_addc_co_u32_e32 v47, vcc, 0, v111, vcc
	global_store_dwordx4 v[46:47], v[54:57], off nt
	v_cvt_pk_bf16_f32 v46, v50, v51
	v_cvt_pk_bf16_f32 v47, v52, v53
	ds_write_b128 v131, v[46:49]
	ds_write_b128 v126, v[38:41]
	ds_read_b128 v[30:33], v130
	ds_read_b128 v[38:41], v130 offset:1024
	v_add_co_u32_e32 v42, vcc, s75, v110
	s_nop 1
	v_addc_co_u32_e32 v43, vcc, 0, v111, vcc
	s_waitcnt lgkmcnt(0)
	global_store_dwordx4 v[42:43], v[30:33], off nt
	s_nop 1
	v_add_co_u32_e32 v30, vcc, s76, v110
	v_cvt_pk_bf16_f32 v32, v26, v27
	v_cvt_pk_bf16_f32 v33, v28, v29
	s_nop 1
	v_addc_co_u32_e32 v31, vcc, 0, v111, vcc
	global_store_dwordx4 v[30:31], v[38:41], off nt
	v_cvt_pk_bf16_f32 v30, v34, v35
	v_cvt_pk_bf16_f32 v31, v36, v37
	ds_write_b128 v131, v[30:33]
	ds_write_b128 v126, v[22:25]
	ds_read_b128 v[14:17], v130
	ds_read_b128 v[22:25], v130 offset:1024
	v_add_co_u32_e32 v26, vcc, s77, v110
	s_nop 1
	v_addc_co_u32_e32 v27, vcc, 0, v111, vcc
	s_waitcnt lgkmcnt(0)
	global_store_dwordx4 v[26:27], v[14:17], off nt
	s_nop 1
	v_add_co_u32_e32 v14, vcc, s78, v110
	v_cvt_pk_bf16_f32 v16, v10, v11
	v_cvt_pk_bf16_f32 v17, v12, v13
	s_nop 1
	v_addc_co_u32_e32 v15, vcc, 0, v111, vcc
	global_store_dwordx4 v[14:15], v[22:25], off nt
	v_cvt_pk_bf16_f32 v14, v18, v19
	v_cvt_pk_bf16_f32 v15, v20, v21
	ds_write_b128 v131, v[14:17]
	ds_write_b128 v126, v[6:9]
	ds_read_b128 v[2:5], v130
	ds_read_b128 v[6:9], v130 offset:1024
	v_add_co_u32_e32 v10, vcc, 0x688000, v110
	s_nop 1
	v_addc_co_u32_e32 v11, vcc, 0, v111, vcc
	s_waitcnt lgkmcnt(0)
	global_store_dwordx4 v[10:11], v[2:5], off nt
	s_nop 1
	v_add_co_u32_e32 v2, vcc, 0x6d4000, v110
	s_nop 1
	v_addc_co_u32_e32 v3, vcc, 0, v111, vcc
	s_andn2_b64 vcc, exec, s[26:27]
	global_store_dwordx4 v[2:3], v[6:9], off nt
	s_cbranch_vccnz .LBB0_336
	s_andn2_b64 vcc, exec, s[16:17]
	s_cbranch_vccnz .LBB0_335
	s_barrier
	s_branch .LBB0_335

.LBB0_372:
	v_mov_b32_e32 v2, v210
	s_nop 15
	s_nop 15
	s_nop 15
	s_add_i32 s0, s65, s56
	v_lshlrev_b32_e32 v5, 7, v2
	v_and_b32_e32 v5, 0x780, v5
	v_ashrrev_i32_e32 v3, 3, v2
	v_and_b32_e32 v4, 7, v2
	v_add_u32_e32 v10, s39, v5
	v_lshrrev_b32_e32 v5, 3, v2
	v_bitop3_b32 v5, v5, v4, s60 bitop3:0x6c
	v_bitop3_b32 v2, v2, v3, 7 bitop3:0x6c
	v_lshlrev_b32_e32 v11, 4, v5
	v_lshlrev_b32_e32 v5, 7, v3
	v_lshlrev_b32_e32 v2, 4, v2
	v_add3_u32 v16, s39, v5, v2
	v_lshl_or_b32 v2, v4, 4, s59
	v_add_u32_e32 v13, s0, v3
	v_lshl_or_b32 v12, s66, 9, v2
	v_pk_mul_f32 v[4:5], v[160:161], s[18:19] op_sel_hi:[1,0]
	v_pk_mul_f32 v[2:3], v[158:159], s[18:19] op_sel_hi:[1,0]
	v_pk_mul_f32 v[6:7], v[156:157], s[18:19] op_sel_hi:[1,0]
	v_pk_mul_f32 v[8:9], v[154:155], s[18:19] op_sel_hi:[1,0]
	v_cvt_pk_bf16_f32 v2, v2, v3
	v_cvt_pk_bf16_f32 v3, v4, v5
	v_cvt_pk_bf16_f32 v5, v6, v7
	v_add_u32_e32 v17, v10, v11
	v_cvt_pk_bf16_f32 v4, v8, v9
	ds_write_b128 v17, v[2:5]
	v_pk_mul_f32 v[4:5], v[152:153], s[18:19] op_sel_hi:[1,0]
	v_pk_mul_f32 v[2:3], v[150:151], s[18:19] op_sel_hi:[1,0]
	v_xad_u32 v18, v11, 16, v10
	v_pk_mul_f32 v[6:7], v[148:149], s[18:19] op_sel_hi:[1,0]
	v_pk_mul_f32 v[8:9], v[146:147], s[18:19] op_sel_hi:[1,0]
	v_cvt_pk_bf16_f32 v2, v2, v3
	v_cvt_pk_bf16_f32 v3, v4, v5
	v_cvt_pk_bf16_f32 v5, v6, v7
	s_nop 0
	v_cvt_pk_bf16_f32 v4, v8, v9
	ds_write_b128 v18, v[2:5]
	ds_read_b128 v[4:7], v16
	ds_read_b128 v[8:11], v16 offset:1024
	v_mad_u64_u32 v[2:3], s[0:1], v13, s61, v[12:13]
	v_mov_b32_e32 v3, v173
	v_lshl_add_u64 v[12:13], s[4:5], 0, v[2:3]
	s_waitcnt lgkmcnt(0)
	global_store_dwordx4 v2, v[4:7], s[4:5] nt
	s_mov_b64 s[0:1], -1
	s_nop 0
	v_add_co_u32_e32 v4, vcc, s62, v12
	v_pk_mul_f32 v[6:7], v[144:145], s[18:19] op_sel_hi:[1,0]
	s_nop 0
	v_addc_co_u32_e32 v5, vcc, 0, v13, vcc
	global_store_dwordx4 v[4:5], v[8:11], off nt
	v_pk_mul_f32 v[4:5], v[142:143], s[18:19] op_sel_hi:[1,0]
	v_add_u32_e32 v12, 0x98000, v2
	v_pk_mul_f32 v[8:9], v[140:141], s[18:19] op_sel_hi:[1,0]
	v_pk_mul_f32 v[10:11], v[138:139], s[18:19] op_sel_hi:[1,0]
	v_cvt_pk_bf16_f32 v4, v4, v5
	v_cvt_pk_bf16_f32 v5, v6, v7
	v_cvt_pk_bf16_f32 v7, v8, v9
	v_pk_mul_f32 v[8:9], v[132:133], s[18:19] op_sel_hi:[1,0]
	v_cvt_pk_bf16_f32 v6, v10, v11
	ds_write_b128 v17, v[4:7]
	v_pk_mul_f32 v[6:7], v[136:137], s[18:19] op_sel_hi:[1,0]
	v_pk_mul_f32 v[4:5], v[134:135], s[18:19] op_sel_hi:[1,0]
	v_pk_mul_f32 v[10:11], v[130:131], s[18:19] op_sel_hi:[1,0]
	v_cvt_pk_bf16_f32 v4, v4, v5
	v_cvt_pk_bf16_f32 v5, v6, v7
	v_cvt_pk_bf16_f32 v7, v8, v9
	v_mov_b32_e32 v13, v173
	v_cvt_pk_bf16_f32 v6, v10, v11
	ds_write_b128 v18, v[4:7]
	ds_read_b128 v[4:7], v16
	ds_read_b128 v[8:11], v16 offset:1024
	v_lshl_add_u64 v[14:15], s[4:5], 0, v[12:13]
	s_waitcnt lgkmcnt(0)
	global_store_dwordx4 v12, v[4:7], s[4:5] nt
	s_nop 1
	v_add_co_u32_e32 v4, vcc, s62, v14
	v_pk_mul_f32 v[6:7], v[128:129], s[18:19] op_sel_hi:[1,0]
	s_nop 0
	v_addc_co_u32_e32 v5, vcc, 0, v15, vcc
	global_store_dwordx4 v[4:5], v[8:11], off nt
	v_pk_mul_f32 v[4:5], v[126:127], s[18:19] op_sel_hi:[1,0]
	v_add_u32_e32 v12, 0x130000, v2
	v_pk_mul_f32 v[8:9], v[124:125], s[18:19] op_sel_hi:[1,0]
	v_pk_mul_f32 v[10:11], v[122:123], s[18:19] op_sel_hi:[1,0]
	v_cvt_pk_bf16_f32 v4, v4, v5
	v_cvt_pk_bf16_f32 v5, v6, v7
	v_cvt_pk_bf16_f32 v7, v8, v9
	v_pk_mul_f32 v[8:9], v[116:117], s[18:19] op_sel_hi:[1,0]
	v_cvt_pk_bf16_f32 v6, v10, v11
	ds_write_b128 v17, v[4:7]
	v_pk_mul_f32 v[6:7], v[120:121], s[18:19] op_sel_hi:[1,0]
	v_pk_mul_f32 v[4:5], v[118:119], s[18:19] op_sel_hi:[1,0]
	v_pk_mul_f32 v[10:11], v[114:115], s[18:19] op_sel_hi:[1,0]
	v_cvt_pk_bf16_f32 v4, v4, v5
	v_cvt_pk_bf16_f32 v5, v6, v7
	v_cvt_pk_bf16_f32 v7, v8, v9
	v_lshl_add_u64 v[14:15], s[4:5], 0, v[12:13]
	v_cvt_pk_bf16_f32 v6, v10, v11
	ds_write_b128 v18, v[4:7]
	ds_read_b128 v[4:7], v16
	ds_read_b128 v[8:11], v16 offset:1024
	s_waitcnt lgkmcnt(0)
	global_store_dwordx4 v12, v[4:7], s[4:5] nt
	s_nop 1
	v_add_co_u32_e32 v4, vcc, s62, v14
	v_pk_mul_f32 v[6:7], v[112:113], s[18:19] op_sel_hi:[1,0]
	s_nop 0
	v_addc_co_u32_e32 v5, vcc, 0, v15, vcc
	global_store_dwordx4 v[4:5], v[8:11], off nt
	v_pk_mul_f32 v[4:5], v[110:111], s[18:19] op_sel_hi:[1,0]
	v_add_u32_e32 v12, 0x1c8000, v2
	v_pk_mul_f32 v[8:9], v[108:109], s[18:19] op_sel_hi:[1,0]
	v_pk_mul_f32 v[10:11], v[106:107], s[18:19] op_sel_hi:[1,0]
	v_cvt_pk_bf16_f32 v4, v4, v5
	v_cvt_pk_bf16_f32 v5, v6, v7
	v_cvt_pk_bf16_f32 v7, v8, v9
	v_pk_mul_f32 v[8:9], v[100:101], s[18:19] op_sel_hi:[1,0]
	v_cvt_pk_bf16_f32 v6, v10, v11
	ds_write_b128 v17, v[4:7]
	v_pk_mul_f32 v[6:7], v[104:105], s[18:19] op_sel_hi:[1,0]
	v_pk_mul_f32 v[4:5], v[102:103], s[18:19] op_sel_hi:[1,0]
	v_pk_mul_f32 v[10:11], v[98:99], s[18:19] op_sel_hi:[1,0]
	v_cvt_pk_bf16_f32 v4, v4, v5
	v_cvt_pk_bf16_f32 v5, v6, v7
	v_cvt_pk_bf16_f32 v7, v8, v9
	v_lshl_add_u64 v[14:15], s[4:5], 0, v[12:13]
	v_cvt_pk_bf16_f32 v6, v10, v11
	ds_write_b128 v18, v[4:7]
	ds_read_b128 v[4:7], v16
	ds_read_b128 v[8:11], v16 offset:1024
	s_waitcnt lgkmcnt(0)
	global_store_dwordx4 v12, v[4:7], s[4:5] nt
	s_nop 1
	v_add_co_u32_e32 v4, vcc, s62, v14
	v_pk_mul_f32 v[6:7], v[96:97], s[18:19] op_sel_hi:[1,0]
	s_nop 0
	v_addc_co_u32_e32 v5, vcc, 0, v15, vcc
	global_store_dwordx4 v[4:5], v[8:11], off nt
	v_pk_mul_f32 v[4:5], v[94:95], s[18:19] op_sel_hi:[1,0]
	v_add_u32_e32 v12, 0x4c0000, v2
	v_pk_mul_f32 v[8:9], v[92:93], s[18:19] op_sel_hi:[1,0]
	v_pk_mul_f32 v[10:11], v[90:91], s[18:19] op_sel_hi:[1,0]
	v_cvt_pk_bf16_f32 v4, v4, v5
	v_cvt_pk_bf16_f32 v5, v6, v7
	v_cvt_pk_bf16_f32 v7, v8, v9
	v_pk_mul_f32 v[8:9], v[84:85], s[18:19] op_sel_hi:[1,0]
	v_cvt_pk_bf16_f32 v6, v10, v11
	ds_write_b128 v17, v[4:7]
	v_pk_mul_f32 v[6:7], v[88:89], s[18:19] op_sel_hi:[1,0]
	v_pk_mul_f32 v[4:5], v[86:87], s[18:19] op_sel_hi:[1,0]
	v_pk_mul_f32 v[10:11], v[82:83], s[18:19] op_sel_hi:[1,0]
	v_cvt_pk_bf16_f32 v4, v4, v5
	v_cvt_pk_bf16_f32 v5, v6, v7
	v_cvt_pk_bf16_f32 v7, v8, v9
	v_lshl_add_u64 v[14:15], s[4:5], 0, v[12:13]
	v_cvt_pk_bf16_f32 v6, v10, v11
	ds_write_b128 v18, v[4:7]
	ds_read_b128 v[4:7], v16
	ds_read_b128 v[8:11], v16 offset:1024
	s_waitcnt lgkmcnt(0)
	global_store_dwordx4 v12, v[4:7], s[4:5] nt
	s_nop 1
	v_add_co_u32_e32 v4, vcc, s62, v14
	v_pk_mul_f32 v[6:7], v[80:81], s[18:19] op_sel_hi:[1,0]
	s_nop 0
	v_addc_co_u32_e32 v5, vcc, 0, v15, vcc
	global_store_dwordx4 v[4:5], v[8:11], off nt
	v_pk_mul_f32 v[4:5], v[78:79], s[18:19] op_sel_hi:[1,0]
	v_add_u32_e32 v12, 0x558000, v2
	v_pk_mul_f32 v[8:9], v[76:77], s[18:19] op_sel_hi:[1,0]
	v_pk_mul_f32 v[10:11], v[74:75], s[18:19] op_sel_hi:[1,0]
	v_cvt_pk_bf16_f32 v4, v4, v5
	v_cvt_pk_bf16_f32 v5, v6, v7
	v_cvt_pk_bf16_f32 v7, v8, v9
	v_pk_mul_f32 v[8:9], v[68:69], s[18:19] op_sel_hi:[1,0]
	v_cvt_pk_bf16_f32 v6, v10, v11
	ds_write_b128 v17, v[4:7]
	v_pk_mul_f32 v[6:7], v[72:73], s[18:19] op_sel_hi:[1,0]
	v_pk_mul_f32 v[4:5], v[70:71], s[18:19] op_sel_hi:[1,0]
	v_pk_mul_f32 v[10:11], v[66:67], s[18:19] op_sel_hi:[1,0]
	v_cvt_pk_bf16_f32 v4, v4, v5
	v_cvt_pk_bf16_f32 v5, v6, v7
	v_cvt_pk_bf16_f32 v7, v8, v9
	v_lshl_add_u64 v[14:15], s[4:5], 0, v[12:13]
	v_cvt_pk_bf16_f32 v6, v10, v11
	ds_write_b128 v18, v[4:7]
	ds_read_b128 v[4:7], v16
	ds_read_b128 v[8:11], v16 offset:1024
	s_waitcnt lgkmcnt(0)
	global_store_dwordx4 v12, v[4:7], s[4:5] nt
	s_nop 1
	v_add_co_u32_e32 v4, vcc, s62, v14
	v_pk_mul_f32 v[6:7], v[64:65], s[18:19] op_sel_hi:[1,0]
	s_nop 0
	v_addc_co_u32_e32 v5, vcc, 0, v15, vcc
	global_store_dwordx4 v[4:5], v[8:11], off nt
	v_pk_mul_f32 v[4:5], v[62:63], s[18:19] op_sel_hi:[1,0]
	v_add_u32_e32 v12, 0x5f0000, v2
	v_pk_mul_f32 v[8:9], v[60:61], s[18:19] op_sel_hi:[1,0]
	v_pk_mul_f32 v[10:11], v[58:59], s[18:19] op_sel_hi:[1,0]
	v_cvt_pk_bf16_f32 v4, v4, v5
	v_cvt_pk_bf16_f32 v5, v6, v7
	v_cvt_pk_bf16_f32 v7, v8, v9
	v_pk_mul_f32 v[8:9], v[52:53], s[18:19] op_sel_hi:[1,0]
	v_cvt_pk_bf16_f32 v6, v10, v11
	ds_write_b128 v17, v[4:7]
	v_pk_mul_f32 v[6:7], v[56:57], s[18:19] op_sel_hi:[1,0]
	v_pk_mul_f32 v[4:5], v[54:55], s[18:19] op_sel_hi:[1,0]
	v_pk_mul_f32 v[10:11], v[50:51], s[18:19] op_sel_hi:[1,0]
	v_cvt_pk_bf16_f32 v4, v4, v5
	v_cvt_pk_bf16_f32 v5, v6, v7
	v_cvt_pk_bf16_f32 v7, v8, v9
	v_lshl_add_u64 v[14:15], s[4:5], 0, v[12:13]
	v_cvt_pk_bf16_f32 v6, v10, v11
	ds_write_b128 v18, v[4:7]
	ds_read_b128 v[4:7], v16
	ds_read_b128 v[8:11], v16 offset:1024
	v_add_u32_e32 v2, 0x688000, v2
	s_waitcnt lgkmcnt(0)
	global_store_dwordx4 v12, v[4:7], s[4:5] nt
	s_nop 1
	v_add_co_u32_e32 v4, vcc, s62, v14
	v_pk_mul_f32 v[6:7], v[48:49], s[18:19] op_sel_hi:[1,0]
	s_nop 0
	v_addc_co_u32_e32 v5, vcc, 0, v15, vcc
	global_store_dwordx4 v[4:5], v[8:11], off nt
	v_pk_mul_f32 v[4:5], v[46:47], s[18:19] op_sel_hi:[1,0]
	v_lshl_add_u64 v[12:13], s[4:5], 0, v[2:3]
	v_pk_mul_f32 v[8:9], v[44:45], s[18:19] op_sel_hi:[1,0]
	v_pk_mul_f32 v[10:11], v[42:43], s[18:19] op_sel_hi:[1,0]
	v_cvt_pk_bf16_f32 v4, v4, v5
	v_cvt_pk_bf16_f32 v5, v6, v7
	v_cvt_pk_bf16_f32 v7, v8, v9
	v_pk_mul_f32 v[8:9], v[36:37], s[18:19] op_sel_hi:[1,0]
	v_cvt_pk_bf16_f32 v6, v10, v11
	ds_write_b128 v17, v[4:7]
	v_pk_mul_f32 v[6:7], v[40:41], s[18:19] op_sel_hi:[1,0]
	v_pk_mul_f32 v[4:5], v[38:39], s[18:19] op_sel_hi:[1,0]
	v_pk_mul_f32 v[10:11], v[34:35], s[18:19] op_sel_hi:[1,0]
	v_cvt_pk_bf16_f32 v4, v4, v5
	v_cvt_pk_bf16_f32 v5, v6, v7
	v_cvt_pk_bf16_f32 v7, v8, v9
	s_nop 0
	v_cvt_pk_bf16_f32 v6, v10, v11
	ds_write_b128 v18, v[4:7]
	ds_read_b128 v[4:7], v16
	ds_read_b128 v[8:11], v16 offset:1024
	s_waitcnt lgkmcnt(0)
	global_store_dwordx4 v2, v[4:7], s[4:5] nt
	v_add_co_u32_e32 v2, vcc, 0x4c000, v12
	s_nop 1
	v_addc_co_u32_e32 v3, vcc, 0, v13, vcc
	s_andn2_b64 vcc, exec, s[24:25]
	global_store_dwordx4 v[2:3], v[8:11], off nt
	s_cbranch_vccnz .LBB0_358
	s_andn2_b64 vcc, exec, s[10:11]
	s_cbranch_vccnz .LBB0_357
	s_barrier
	s_branch .LBB0_357

.LBB0_619:
	v_mov_b32_e32 v2, v197
	s_nop 15
	s_nop 15
	s_nop 15
	s_add_i32 s0, s63, s54
	v_lshlrev_b32_e32 v5, 7, v2
	v_and_b32_e32 v5, 0x780, v5
	v_ashrrev_i32_e32 v3, 3, v2
	v_and_b32_e32 v4, 7, v2
	v_add_u32_e32 v10, s39, v5
	v_lshrrev_b32_e32 v5, 3, v2
	v_bitop3_b32 v5, v5, v4, s58 bitop3:0x6c
	v_bitop3_b32 v2, v2, v3, 7 bitop3:0x6c
	v_lshlrev_b32_e32 v11, 4, v5
	v_lshlrev_b32_e32 v5, 7, v3
	v_lshlrev_b32_e32 v2, 4, v2
	v_add3_u32 v16, s39, v5, v2
	v_lshl_or_b32 v2, v4, 4, s57
	v_add_u32_e32 v13, s0, v3
	v_lshl_or_b32 v12, s24, 9, v2
	v_pk_mul_f32 v[4:5], v[160:161], s[16:17] op_sel_hi:[1,0]
	v_pk_mul_f32 v[2:3], v[158:159], s[16:17] op_sel_hi:[1,0]
	v_pk_mul_f32 v[6:7], v[156:157], s[16:17] op_sel_hi:[1,0]
	v_pk_mul_f32 v[8:9], v[154:155], s[16:17] op_sel_hi:[1,0]
	v_cvt_pk_bf16_f32 v2, v2, v3
	v_cvt_pk_bf16_f32 v3, v4, v5
	v_cvt_pk_bf16_f32 v5, v6, v7
	v_add_u32_e32 v17, v10, v11
	v_cvt_pk_bf16_f32 v4, v8, v9
	ds_write_b128 v17, v[2:5]
	v_pk_mul_f32 v[4:5], v[152:153], s[16:17] op_sel_hi:[1,0]
	v_pk_mul_f32 v[2:3], v[150:151], s[16:17] op_sel_hi:[1,0]
	v_xad_u32 v18, v11, 16, v10
	v_pk_mul_f32 v[6:7], v[148:149], s[16:17] op_sel_hi:[1,0]
	v_pk_mul_f32 v[8:9], v[146:147], s[16:17] op_sel_hi:[1,0]
	v_cvt_pk_bf16_f32 v2, v2, v3
	v_cvt_pk_bf16_f32 v3, v4, v5
	v_cvt_pk_bf16_f32 v5, v6, v7
	s_nop 0
	v_cvt_pk_bf16_f32 v4, v8, v9
	ds_write_b128 v18, v[2:5]
	ds_read_b128 v[4:7], v16
	ds_read_b128 v[8:11], v16 offset:1024
	v_mad_u64_u32 v[2:3], s[0:1], v13, s59, v[12:13]
	v_mov_b32_e32 v3, v173
	v_lshl_add_u64 v[12:13], s[4:5], 0, v[2:3]
	s_waitcnt lgkmcnt(0)
	global_store_dwordx4 v2, v[4:7], s[4:5] nt
	s_mov_b64 s[0:1], -1
	s_nop 0
	v_add_co_u32_e32 v4, vcc, s60, v12
	v_pk_mul_f32 v[6:7], v[144:145], s[16:17] op_sel_hi:[1,0]
	s_nop 0
	v_addc_co_u32_e32 v5, vcc, 0, v13, vcc
	global_store_dwordx4 v[4:5], v[8:11], off nt
	v_pk_mul_f32 v[4:5], v[142:143], s[16:17] op_sel_hi:[1,0]
	v_add_u32_e32 v12, 0x98000, v2
	v_pk_mul_f32 v[8:9], v[140:141], s[16:17] op_sel_hi:[1,0]
	v_pk_mul_f32 v[10:11], v[138:139], s[16:17] op_sel_hi:[1,0]
	v_cvt_pk_bf16_f32 v4, v4, v5
	v_cvt_pk_bf16_f32 v5, v6, v7
	v_cvt_pk_bf16_f32 v7, v8, v9
	v_pk_mul_f32 v[8:9], v[132:133], s[16:17] op_sel_hi:[1,0]
	v_cvt_pk_bf16_f32 v6, v10, v11
	ds_write_b128 v17, v[4:7]
	v_pk_mul_f32 v[6:7], v[136:137], s[16:17] op_sel_hi:[1,0]
	v_pk_mul_f32 v[4:5], v[134:135], s[16:17] op_sel_hi:[1,0]
	v_pk_mul_f32 v[10:11], v[130:131], s[16:17] op_sel_hi:[1,0]
	v_cvt_pk_bf16_f32 v4, v4, v5
	v_cvt_pk_bf16_f32 v5, v6, v7
	v_cvt_pk_bf16_f32 v7, v8, v9
	v_mov_b32_e32 v13, v173
	v_cvt_pk_bf16_f32 v6, v10, v11
	ds_write_b128 v18, v[4:7]
	ds_read_b128 v[4:7], v16
	ds_read_b128 v[8:11], v16 offset:1024
	v_lshl_add_u64 v[14:15], s[4:5], 0, v[12:13]
	s_waitcnt lgkmcnt(0)
	global_store_dwordx4 v12, v[4:7], s[4:5] nt
	s_nop 1
	v_add_co_u32_e32 v4, vcc, s60, v14
	v_pk_mul_f32 v[6:7], v[128:129], s[16:17] op_sel_hi:[1,0]
	s_nop 0
	v_addc_co_u32_e32 v5, vcc, 0, v15, vcc
	global_store_dwordx4 v[4:5], v[8:11], off nt
	v_pk_mul_f32 v[4:5], v[126:127], s[16:17] op_sel_hi:[1,0]
	v_add_u32_e32 v12, 0x130000, v2
	v_pk_mul_f32 v[8:9], v[124:125], s[16:17] op_sel_hi:[1,0]
	v_pk_mul_f32 v[10:11], v[122:123], s[16:17] op_sel_hi:[1,0]
	v_cvt_pk_bf16_f32 v4, v4, v5
	v_cvt_pk_bf16_f32 v5, v6, v7
	v_cvt_pk_bf16_f32 v7, v8, v9
	v_pk_mul_f32 v[8:9], v[116:117], s[16:17] op_sel_hi:[1,0]
	v_cvt_pk_bf16_f32 v6, v10, v11
	ds_write_b128 v17, v[4:7]
	v_pk_mul_f32 v[6:7], v[120:121], s[16:17] op_sel_hi:[1,0]
	v_pk_mul_f32 v[4:5], v[118:119], s[16:17] op_sel_hi:[1,0]
	v_pk_mul_f32 v[10:11], v[114:115], s[16:17] op_sel_hi:[1,0]
	v_cvt_pk_bf16_f32 v4, v4, v5
	v_cvt_pk_bf16_f32 v5, v6, v7
	v_cvt_pk_bf16_f32 v7, v8, v9
	v_lshl_add_u64 v[14:15], s[4:5], 0, v[12:13]
	v_cvt_pk_bf16_f32 v6, v10, v11
	ds_write_b128 v18, v[4:7]
	ds_read_b128 v[4:7], v16
	ds_read_b128 v[8:11], v16 offset:1024
	s_waitcnt lgkmcnt(0)
	global_store_dwordx4 v12, v[4:7], s[4:5] nt
	s_nop 1
	v_add_co_u32_e32 v4, vcc, s60, v14
	v_pk_mul_f32 v[6:7], v[112:113], s[16:17] op_sel_hi:[1,0]
	s_nop 0
	v_addc_co_u32_e32 v5, vcc, 0, v15, vcc
	global_store_dwordx4 v[4:5], v[8:11], off nt
	v_pk_mul_f32 v[4:5], v[110:111], s[16:17] op_sel_hi:[1,0]
	v_add_u32_e32 v12, 0x1c8000, v2
	v_pk_mul_f32 v[8:9], v[108:109], s[16:17] op_sel_hi:[1,0]
	v_pk_mul_f32 v[10:11], v[106:107], s[16:17] op_sel_hi:[1,0]
	v_cvt_pk_bf16_f32 v4, v4, v5
	v_cvt_pk_bf16_f32 v5, v6, v7
	v_cvt_pk_bf16_f32 v7, v8, v9
	v_pk_mul_f32 v[8:9], v[100:101], s[16:17] op_sel_hi:[1,0]
	v_cvt_pk_bf16_f32 v6, v10, v11
	ds_write_b128 v17, v[4:7]
	v_pk_mul_f32 v[6:7], v[104:105], s[16:17] op_sel_hi:[1,0]
	v_pk_mul_f32 v[4:5], v[102:103], s[16:17] op_sel_hi:[1,0]
	v_pk_mul_f32 v[10:11], v[98:99], s[16:17] op_sel_hi:[1,0]
	v_cvt_pk_bf16_f32 v4, v4, v5
	v_cvt_pk_bf16_f32 v5, v6, v7
	v_cvt_pk_bf16_f32 v7, v8, v9
	v_lshl_add_u64 v[14:15], s[4:5], 0, v[12:13]
	v_cvt_pk_bf16_f32 v6, v10, v11
	ds_write_b128 v18, v[4:7]
	ds_read_b128 v[4:7], v16
	ds_read_b128 v[8:11], v16 offset:1024
	s_waitcnt lgkmcnt(0)
	global_store_dwordx4 v12, v[4:7], s[4:5] nt
	s_nop 1
	v_add_co_u32_e32 v4, vcc, s60, v14
	v_pk_mul_f32 v[6:7], v[96:97], s[16:17] op_sel_hi:[1,0]
	s_nop 0
	v_addc_co_u32_e32 v5, vcc, 0, v15, vcc
	global_store_dwordx4 v[4:5], v[8:11], off nt
	v_pk_mul_f32 v[4:5], v[94:95], s[16:17] op_sel_hi:[1,0]
	v_add_u32_e32 v12, 0x4c0000, v2
	v_pk_mul_f32 v[8:9], v[92:93], s[16:17] op_sel_hi:[1,0]
	v_pk_mul_f32 v[10:11], v[90:91], s[16:17] op_sel_hi:[1,0]
	v_cvt_pk_bf16_f32 v4, v4, v5
	v_cvt_pk_bf16_f32 v5, v6, v7
	v_cvt_pk_bf16_f32 v7, v8, v9
	v_pk_mul_f32 v[8:9], v[84:85], s[16:17] op_sel_hi:[1,0]
	v_cvt_pk_bf16_f32 v6, v10, v11
	ds_write_b128 v17, v[4:7]
	v_pk_mul_f32 v[6:7], v[88:89], s[16:17] op_sel_hi:[1,0]
	v_pk_mul_f32 v[4:5], v[86:87], s[16:17] op_sel_hi:[1,0]
	v_pk_mul_f32 v[10:11], v[82:83], s[16:17] op_sel_hi:[1,0]
	v_cvt_pk_bf16_f32 v4, v4, v5
	v_cvt_pk_bf16_f32 v5, v6, v7
	v_cvt_pk_bf16_f32 v7, v8, v9
	v_lshl_add_u64 v[14:15], s[4:5], 0, v[12:13]
	v_cvt_pk_bf16_f32 v6, v10, v11
	ds_write_b128 v18, v[4:7]
	ds_read_b128 v[4:7], v16
	ds_read_b128 v[8:11], v16 offset:1024
	s_waitcnt lgkmcnt(0)
	global_store_dwordx4 v12, v[4:7], s[4:5] nt
	s_nop 1
	v_add_co_u32_e32 v4, vcc, s60, v14
	v_pk_mul_f32 v[6:7], v[80:81], s[16:17] op_sel_hi:[1,0]
	s_nop 0
	v_addc_co_u32_e32 v5, vcc, 0, v15, vcc
	global_store_dwordx4 v[4:5], v[8:11], off nt
	v_pk_mul_f32 v[4:5], v[78:79], s[16:17] op_sel_hi:[1,0]
	v_add_u32_e32 v12, 0x558000, v2
	v_pk_mul_f32 v[8:9], v[76:77], s[16:17] op_sel_hi:[1,0]
	v_pk_mul_f32 v[10:11], v[74:75], s[16:17] op_sel_hi:[1,0]
	v_cvt_pk_bf16_f32 v4, v4, v5
	v_cvt_pk_bf16_f32 v5, v6, v7
	v_cvt_pk_bf16_f32 v7, v8, v9
	v_pk_mul_f32 v[8:9], v[68:69], s[16:17] op_sel_hi:[1,0]
	v_cvt_pk_bf16_f32 v6, v10, v11
	ds_write_b128 v17, v[4:7]
	v_pk_mul_f32 v[6:7], v[72:73], s[16:17] op_sel_hi:[1,0]
	v_pk_mul_f32 v[4:5], v[70:71], s[16:17] op_sel_hi:[1,0]
	v_pk_mul_f32 v[10:11], v[66:67], s[16:17] op_sel_hi:[1,0]
	v_cvt_pk_bf16_f32 v4, v4, v5
	v_cvt_pk_bf16_f32 v5, v6, v7
	v_cvt_pk_bf16_f32 v7, v8, v9
	v_lshl_add_u64 v[14:15], s[4:5], 0, v[12:13]
	v_cvt_pk_bf16_f32 v6, v10, v11
	ds_write_b128 v18, v[4:7]
	ds_read_b128 v[4:7], v16
	ds_read_b128 v[8:11], v16 offset:1024
	s_waitcnt lgkmcnt(0)
	global_store_dwordx4 v12, v[4:7], s[4:5] nt
	s_nop 1
	v_add_co_u32_e32 v4, vcc, s60, v14
	v_pk_mul_f32 v[6:7], v[64:65], s[16:17] op_sel_hi:[1,0]
	s_nop 0
	v_addc_co_u32_e32 v5, vcc, 0, v15, vcc
	global_store_dwordx4 v[4:5], v[8:11], off nt
	v_pk_mul_f32 v[4:5], v[62:63], s[16:17] op_sel_hi:[1,0]
	v_add_u32_e32 v12, 0x5f0000, v2
	v_pk_mul_f32 v[8:9], v[60:61], s[16:17] op_sel_hi:[1,0]
	v_pk_mul_f32 v[10:11], v[58:59], s[16:17] op_sel_hi:[1,0]
	v_cvt_pk_bf16_f32 v4, v4, v5
	v_cvt_pk_bf16_f32 v5, v6, v7
	v_cvt_pk_bf16_f32 v7, v8, v9
	v_pk_mul_f32 v[8:9], v[52:53], s[16:17] op_sel_hi:[1,0]
	v_cvt_pk_bf16_f32 v6, v10, v11
	ds_write_b128 v17, v[4:7]
	v_pk_mul_f32 v[6:7], v[56:57], s[16:17] op_sel_hi:[1,0]
	v_pk_mul_f32 v[4:5], v[54:55], s[16:17] op_sel_hi:[1,0]
	v_pk_mul_f32 v[10:11], v[50:51], s[16:17] op_sel_hi:[1,0]
	v_cvt_pk_bf16_f32 v4, v4, v5
	v_cvt_pk_bf16_f32 v5, v6, v7
	v_cvt_pk_bf16_f32 v7, v8, v9
	v_lshl_add_u64 v[14:15], s[4:5], 0, v[12:13]
	v_cvt_pk_bf16_f32 v6, v10, v11
	ds_write_b128 v18, v[4:7]
	ds_read_b128 v[4:7], v16
	ds_read_b128 v[8:11], v16 offset:1024
	v_add_u32_e32 v2, 0x688000, v2
	s_waitcnt lgkmcnt(0)
	global_store_dwordx4 v12, v[4:7], s[4:5] nt
	s_nop 1
	v_add_co_u32_e32 v4, vcc, s60, v14
	v_pk_mul_f32 v[6:7], v[48:49], s[16:17] op_sel_hi:[1,0]
	s_nop 0
	v_addc_co_u32_e32 v5, vcc, 0, v15, vcc
	global_store_dwordx4 v[4:5], v[8:11], off nt
	v_pk_mul_f32 v[4:5], v[46:47], s[16:17] op_sel_hi:[1,0]
	v_lshl_add_u64 v[12:13], s[4:5], 0, v[2:3]
	v_pk_mul_f32 v[8:9], v[44:45], s[16:17] op_sel_hi:[1,0]
	v_pk_mul_f32 v[10:11], v[42:43], s[16:17] op_sel_hi:[1,0]
	v_cvt_pk_bf16_f32 v4, v4, v5
	v_cvt_pk_bf16_f32 v5, v6, v7
	v_cvt_pk_bf16_f32 v7, v8, v9
	v_pk_mul_f32 v[8:9], v[36:37], s[16:17] op_sel_hi:[1,0]
	v_cvt_pk_bf16_f32 v6, v10, v11
	ds_write_b128 v17, v[4:7]
	v_pk_mul_f32 v[6:7], v[40:41], s[16:17] op_sel_hi:[1,0]
	v_pk_mul_f32 v[4:5], v[38:39], s[16:17] op_sel_hi:[1,0]
	v_pk_mul_f32 v[10:11], v[34:35], s[16:17] op_sel_hi:[1,0]
	v_cvt_pk_bf16_f32 v4, v4, v5
	v_cvt_pk_bf16_f32 v5, v6, v7
	v_cvt_pk_bf16_f32 v7, v8, v9
	s_nop 0
	v_cvt_pk_bf16_f32 v6, v10, v11
	ds_write_b128 v18, v[4:7]
	ds_read_b128 v[4:7], v16
	ds_read_b128 v[8:11], v16 offset:1024
	s_waitcnt lgkmcnt(0)
	global_store_dwordx4 v2, v[4:7], s[4:5] nt
	v_add_co_u32_e32 v2, vcc, 0x4c000, v12
	s_nop 1
	v_addc_co_u32_e32 v3, vcc, 0, v13, vcc
	s_andn2_b64 vcc, exec, s[22:23]
	global_store_dwordx4 v[2:3], v[8:11], off nt
	s_cbranch_vccnz .LBB0_605
	s_andn2_b64 vcc, exec, s[8:9]
	s_cbranch_vccnz .LBB0_604
	s_barrier
	s_branch .LBB0_604
